# attention: K/V tiles by LDS-DMA (K 2 ahead, V 1 ahead), one barrier per 64-key tile, register staging + ds_write removed
# speedup vs baseline: 1.0111x; 1.0111x over previous
.LBB0_1343:
	s_and_b32 s3, s21, 3
	s_and_b64 s[4:5], exec, s[34:35]
	s_cselect_b32 s3, -1, s3
	s_cmp_eq_u32 s3, 2
	s_movk_i32 s4, 0x3080
	s_cselect_b32 s4, 0x2000, s4
	s_cmp_lg_u32 s3, 1
	s_cselect_b32 s4, s4, 0x1000
	s_cmp_gt_i32 s3, 0
	s_cselect_b32 s8, s4, 0
	s_mul_i32 s18, s8, 0xe00
	v_readlane_b32 s4, v253, 7
	v_readlane_b32 s5, v253, 8
	s_add_u32 s4, s4, s18
	v_lshlrev_b32_e32 v2, 8, v181
	v_mov_b32_e32 v3, v99
	v_lshl_add_u32 v7, v7, 7, v14
	s_addc_u32 s5, s5, 0
	v_lshlrev_b64 v[50:51], 1, v[2:3]
	v_cvt_pk_bf16_f32 v5, v5, v99
	ds_write_b16 v7, v5
	v_cvt_pk_bf16_f32 v4, v4, v99
	v_lshl_add_u64 v[2:3], s[4:5], 0, v[50:51]
	ds_write_b16 v7, v4 offset:32
	v_ashrrev_i32_e32 v4, 4, v6
	v_lshlrev_b32_e32 v5, 3, v6
	s_movk_i32 s4, 0x700
	v_and_b32_e32 v7, 0x78, v5
	v_mul_lo_u32 v8, v4, s4
	v_or_b32_e32 v8, v8, v7
	v_lshlrev_b32_e32 v52, 1, v8
	v_readfirstlane_b32 s4, v2
	v_readfirstlane_b32 s5, v3
	s_waitcnt lgkmcnt(0)
	s_barrier
	v_add_u32_e32 v54, 0x1c000, v52
	s_nop 1
	global_load_dwordx4 v[8:11], v52, s[4:5] offset:1792
	global_load_dwordx4 v[14:17], v54, s[4:5] offset:1792
	s_lshl_b32 s22, s8, 7
	v_readlane_b32 s8, v253, 5
	v_lshlrev_b32_e32 v26, 4, v6
	v_readlane_b32 s9, v253, 6
	s_add_u32 s24, s8, s22
	v_ashrrev_i32_e32 v13, 3, v6
	v_and_b32_e32 v30, 0x70, v26
	s_addc_u32 s25, s9, 0
	v_lshl_or_b32 v56, v13, 7, v30
	global_load_dwordx4 v[18:21], v52, s[4:5] offset:1536
	global_load_dwordx4 v[22:25], v54, s[4:5] offset:1536
	global_load_dwordx4 v[26:29], v56, s[24:25]
	v_lshlrev_b32_e32 v31, 7, v194
	v_lshlrev_b32_e32 v12, 1, v12
	v_readlane_b32 s4, v255, 34
	v_lshlrev_b32_e32 v32, 1, v4
	v_lshrrev_b32_e32 v33, 1, v4
	v_add3_u32 v12, s4, v31, v12
	v_and_b32_e32 v31, 0xfffff0, v4
	v_and_b32_e32 v35, 3, v4
	v_add_u32_e32 v36, 32, v4
	s_add_i32 s4, 0, 0x14000
	ds_read_b128 v[144:147], v12
	ds_read_b128 v[140:143], v12 offset:32
	ds_read_b128 v[136:139], v12 offset:64
	ds_read_b128 v[132:135], v12 offset:96
	v_and_or_b32 v12, v32, 8, v31
	v_and_or_b32 v31, v33, 4, v35
	v_and_b32_e32 v32, 0xfffff0, v36
	v_lshlrev_b32_e32 v33, 1, v36
	s_and_b64 s[0:1], s[0:1], exec
	v_bfe_u32 v34, v5, 5, 2
	v_lshrrev_b32_e32 v12, 1, v12
	v_and_or_b32 v32, v33, 8, v32
	s_cselect_b32 s5, 0x104, 4
	s_cmp_lt_u32 s3, 2
	v_lshlrev_b32_e32 v7, 1, v7
	v_or_b32_e32 v12, v12, v34
	v_lshrrev_b32_e32 v32, 1, v32
	s_cselect_b32 s3, 64, 0x42
	s_and_b64 s[0:1], exec, s[34:35]
	v_lshlrev_b32_e32 v31, 6, v31
	v_and_b32_e32 v35, 48, v7
	v_lshlrev_b32_e32 v12, 9, v12
	v_or_b32_e32 v32, v32, v34
	s_cselect_b32 s3, s5, s3
	s_add_i32 s0, 0, 0x8000
	v_lshlrev_b32_e32 v32, 9, v32
	v_or3_b32 v12, v12, v31, v35
	s_cmp_lg_u32 s0, -1
	v_or3_b32 v31, v32, v31, v35
	v_add_u32_e32 v205, 0, v12
	s_cselect_b32 s0, s0, 0
	s_movk_i32 s8, 0x70
	v_add_u32_e32 v206, 0, v31
	s_waitcnt vmcnt(0)
	v_mov_b32_e32 v12, s0
	s_movk_i32 s0, 0x180
	v_mul_lo_u32 v4, v4, s0
	v_bitop3_b32 v37, v98, v5, s8 bitop3:0x78
	s_waitcnt vmcnt(4)
	ds_write_b128 v205, v[8:11]
	s_waitcnt vmcnt(3)
	ds_write_b128 v206, v[14:17]
	v_lshrrev_b32_e32 v8, 1, v6
	v_bitop3_b32 v7, v7, v8, s8 bitop3:0x78
	v_add3_u32 v207, v7, v4, 0
	v_mul_lo_u32 v4, v13, s0
	v_or_b32_e32 v7, 0x100, v30
	v_and_b32_e32 v8, 0x70, v6
	v_mad_u32_u24 v53, v195, s0, v12
	v_xad_u32 v4, v7, v8, v4
	v_add_u32_e32 v201, v37, v53
	v_add_u32_e32 v208, 0, v4
	s_waitcnt vmcnt(2)
	ds_write_b128 v207, v[18:21] offset:32768
	s_waitcnt vmcnt(1)
	ds_write_b128 v207, v[22:25] offset:45056
	s_waitcnt vmcnt(0)
	ds_write_b128 v208, v[26:29] offset:32768
	s_waitcnt lgkmcnt(0)
	s_barrier
	ds_read_b128 v[8:11], v201
	ds_read_b128 v[12:15], v201 offset:128
	s_waitcnt lgkmcnt(1)
	v_mfma_f32_32x32x16_bf16 v[18:33], v[8:11], v[128:131], 0
	ds_read_b128 v[8:11], v201 offset:12288
	ds_read_b128 v[60:63], v201 offset:256
	v_and_b32_e32 v4, 0x70, v5
	v_bitop3_b32 v5, v98, v4, 32 bitop3:0x36
	v_add_u32_e32 v203, v5, v53
	v_bitop3_b32 v5, v98, v4, 64 bitop3:0x36
	v_add_u32_e32 v204, v5, v53
	s_waitcnt lgkmcnt(1)
	v_mfma_f32_32x32x16_bf16 v[34:49], v[8:11], v[128:131], 0
	ds_read_b128 v[8:11], v203
	ds_read_b128 v[64:67], v203 offset:128
	ds_read_b128 v[68:71], v203 offset:256
	s_movk_i32 s0, 0x60
	v_bitop3_b32 v4, v98, v4, s0 bitop3:0x36
	v_add_u32_e32 v202, v4, v53
	s_mov_b64 s[0:1], 0x38700
	v_lshl_add_u64 v[4:5], v[2:3], 0, s[0:1]
	s_waitcnt lgkmcnt(2)
	v_mfma_f32_32x32x16_bf16 v[18:33], v[8:11], v[124:127], v[18:33]
	ds_read_b128 v[8:11], v203 offset:12288
	s_mov_b64 s[0:1], 0x38600
	v_lshl_add_u64 v[2:3], v[2:3], 0, s[0:1]
	v_readfirstlane_b32 s0, v4
	v_readfirstlane_b32 s1, v5
	v_readfirstlane_b32 s8, v2
	v_readfirstlane_b32 s9, v3
	s_waitcnt lgkmcnt(0)
	v_mfma_f32_32x32x16_bf16 v[34:49], v[8:11], v[124:127], v[34:49]
	ds_read_b128 v[8:11], v204
	ds_read_b128 v[72:75], v204 offset:128
	ds_read_b128 v[76:79], v204 offset:256
	v_mov_b32_e32 v57, v99
	v_add_u32_e32 v209, 0x3000, v207
	s_cmp_lg_u32 0, -1
	v_lshlrev_b32_e32 v4, 1, v58
	v_and_b32_e32 v4, 32, v4
	s_waitcnt lgkmcnt(2)
	v_mfma_f32_32x32x16_bf16 v[18:33], v[8:11], v[120:123], v[18:33]
	ds_read_b128 v[8:11], v204 offset:12288
	s_mov_b32 s36, s63
	s_mov_b32 s37, s63
	s_mov_b32 s19, s63
	s_mov_b32 s38, s63
	s_mov_b32 s39, s63
	s_mov_b32 s40, s63
	s_waitcnt lgkmcnt(0)
	v_mfma_f32_32x32x16_bf16 v[34:49], v[8:11], v[120:123], v[34:49]
	ds_read_b128 v[8:11], v202
	ds_read_b128 v[80:83], v202 offset:128
	s_mov_b32 s41, s63
	s_mov_b32 s42, s63
	s_mov_b32 s43, s63
	s_mov_b32 s44, s63
	s_mov_b32 s45, s63
	s_mov_b32 s46, s63
	s_waitcnt lgkmcnt(1)
	v_mfma_f32_32x32x16_bf16 v[18:33], v[8:11], v[116:119], v[18:33]
	ds_read_b128 v[8:11], v202 offset:12288
	ds_read_b128 v[84:87], v202 offset:256
	s_mov_b32 s47, s63
	s_mov_b32 s48, s63
	s_mov_b32 s49, s63
	s_mov_b32 s50, s63
	s_mov_b32 s51, s63
	s_mov_b32 s23, s63
	v_mfma_f32_32x32x16_bf16 v[18:33], v[12:15], v[112:115], v[18:33]
	v_mov_b32_e32 v53, v99
	v_mov_b32_e32 v55, v99
	v_lshl_add_u64 v[182:183], s[22:23], 0, v[56:57]
	v_mov_b32_e32 v227, 0x3200
	v_mov_b32_e32 v199, 0
	s_waitcnt lgkmcnt(1)
	v_mfma_f32_32x32x16_bf16 v[34:49], v[8:11], v[116:119], v[34:49]
	ds_read_b128 v[8:11], v201 offset:12416
	ds_read_b128 v[12:15], v201 offset:12544
	v_mfma_f32_32x32x16_bf16 v[18:33], v[64:67], v[108:111], v[18:33]
	s_waitcnt lgkmcnt(1)
	v_mfma_f32_32x32x16_bf16 v[34:49], v[8:11], v[112:115], v[34:49]
	ds_read_b128 v[8:11], v203 offset:12416
	ds_read_b128 v[64:67], v203 offset:12544
	v_mfma_f32_32x32x16_bf16 v[18:33], v[72:75], v[104:107], v[18:33]
	s_waitcnt lgkmcnt(1)
	v_mfma_f32_32x32x16_bf16 v[34:49], v[8:11], v[108:111], v[34:49]
	ds_read_b128 v[8:11], v204 offset:12416
	ds_read_b128 v[72:75], v204 offset:12544
	v_mfma_f32_32x32x16_bf16 v[18:33], v[80:83], v[100:103], v[18:33]
	s_waitcnt lgkmcnt(1)
	v_mfma_f32_32x32x16_bf16 v[34:49], v[8:11], v[104:107], v[34:49]
	ds_read_b128 v[8:11], v202 offset:12416
	ds_read_b128 v[80:83], v202 offset:12544
	v_mfma_f32_32x32x16_bf16 v[18:33], v[60:63], v[144:147], v[18:33]
	global_load_dwordx4 v[60:63], v54, s[0:1]
	global_load_dwordx4 v[88:91], v52, s[8:9]
	global_load_dwordx4 v[92:95], v52, s[0:1]
	global_load_dwordx4 v[148:151], v54, s[8:9]
	s_movk_i32 s0, 0x2000
	s_mov_b32 s8, 2
	s_waitcnt lgkmcnt(1)
	v_mfma_f32_32x32x16_bf16 v[34:49], v[8:11], v[100:103], v[34:49]
	v_lshl_add_u64 v[8:9], s[24:25], 0, v[56:57]
	v_add_co_u32_e32 v2, vcc, s0, v8
	v_cmp_gt_u32_e64 s[0:1], 32, v58
	s_nop 0
	v_addc_co_u32_e32 v3, vcc, 0, v9, vcc
	global_load_dwordx4 v[152:155], v[2:3], off
	v_mfma_f32_32x32x16_bf16 v[18:33], v[68:71], v[140:143], v[18:33]
	s_waitcnt vmcnt(0)
	s_waitcnt vmcnt(2)
	ds_write_b128 v205, v[92:95] offset:16384
	ds_write_b128 v206, v[60:63] offset:16384
	ds_write_b128 v207, v[88:91] offset:57344
	s_waitcnt vmcnt(1)
	ds_write_b128 v209, v[148:151] offset:57344
	s_waitcnt vmcnt(0)
	ds_write_b128 v208, v[152:155] offset:57344
	v_mfma_f32_32x32x16_bf16 v[34:49], v[12:15], v[144:147], v[34:49]
	v_and_b32_e32 v2, 0x3fffffc0, v6
	v_lshl_add_u32 v196, v2, 2, s4
	s_cselect_b32 s4, 0, 0
	v_lshlrev_b32_e32 v3, 4, v58
	v_lshlrev_b32_e32 v2, 3, v58
	v_and_b32_e32 v3, 0xc0, v3
	v_and_or_b32 v3, v2, 24, v3
	v_mfma_f32_32x32x16_bf16 v[18:33], v[76:79], v[136:139], v[18:33]
	v_and_b32_e32 v2, 0x100, v2
	v_or3_b32 v59, v3, v4, v2
	v_mov_b64_e32 v[2:3], s[36:37]
	v_add_u32_e32 v200, s4, v59
	v_mov_b64_e32 v[16:17], s[50:51]
	v_mov_b64_e32 v[4:5], s[38:39]
	v_mov_b64_e32 v[6:7], s[40:41]
	v_mfma_f32_32x32x16_bf16 v[34:49], v[64:67], v[140:143], v[34:49]
	v_mov_b64_e32 v[8:9], s[42:43]
	v_mov_b64_e32 v[10:11], s[44:45]
	v_mov_b64_e32 v[12:13], s[46:47]
	v_mov_b64_e32 v[14:15], s[48:49]
	v_lshl_add_u32 v197, v195, 2, v196
	s_waitcnt lgkmcnt(0)
	s_barrier
	v_mfma_f32_32x32x16_bf16 v[18:33], v[84:87], v[132:135], v[18:33]
	v_mfma_f32_32x32x16_bf16 v[34:49], v[72:75], v[136:139], v[34:49]
	s_nop 10
	v_max_f32_e32 v64, v19, v19
	v_max_f32_e32 v65, v18, v18
	v_max_f32_e32 v64, v65, v64
	v_max3_f32 v64, v64, v20, v21
	v_max3_f32 v64, v64, v22, v23
	v_max3_f32 v64, v64, v24, v25
	v_max3_f32 v64, v64, v26, v27
	v_mfma_f32_32x32x16_bf16 v[34:49], v[80:83], v[132:135], v[34:49]
	v_max3_f32 v64, v64, v28, v29
	v_max3_f32 v64, v64, v30, v31
	v_max3_f32 v64, v64, v32, v33
	s_nop 8
	v_max3_f32 v64, v64, v34, v35
	v_max3_f32 v64, v64, v36, v37
	v_max3_f32 v64, v64, v38, v39
	v_max3_f32 v64, v64, v40, v41
	v_max3_f32 v64, v64, v42, v43
	v_max3_f32 v64, v64, v44, v45
	v_max3_f32 v64, v64, v46, v47
	v_max3_f32 v64, v64, v48, v49
	v_mov_b32_e32 v65, v64
	s_nop 1
	v_permlane32_swap_b32_e32 v64, v65
	v_max_f32_e32 v65, v65, v65
	v_max_f32_e32 v64, v64, v64
	v_max_f32_e32 v64, v64, v65
	v_max_f32_e32 v60, 0xf149f2ca, v64
	v_sub_f32_e32 v61, 0xf149f2ca, v60
	v_mul_f32_e32 v61, 0x3dd53b94, v61
	v_add_f32_e32 v65, 0x7149f2ca, v64
	v_exp_f32_e32 v61, v61
	v_cmp_ge_f32_e32 vcc, s11, v65
	s_cmp_eq_u64 vcc, exec
	s_cselect_b64 vcc, -1, 0
	v_cndmask_b32_e64 v210, v61, 1.0, vcc
	v_mov_b32_e32 v61, 0xf149f2ca
	v_cndmask_b32_e32 v211, v60, v61, vcc
	v_mul_f32_e32 v60, 0xbdd53b94, v211
	v_fmamk_f32 v18, v18, 0x3dd53b94, v60
	v_exp_f32_e32 v169, v18
	v_fmamk_f32 v18, v19, 0x3dd53b94, v60
	v_exp_f32_e32 v191, v18
	v_fmamk_f32 v18, v20, 0x3dd53b94, v60
	v_exp_f32_e32 v170, v18
	v_fmamk_f32 v18, v21, 0x3dd53b94, v60
	v_exp_f32_e32 v192, v18
	v_fmamk_f32 v18, v22, 0x3dd53b94, v60
	v_exp_f32_e32 v190, v18
	v_fmamk_f32 v18, v23, 0x3dd53b94, v60
	v_exp_f32_e32 v193, v18
	v_fmamk_f32 v18, v24, 0x3dd53b94, v60
	v_exp_f32_e32 v171, v18
	v_fmamk_f32 v18, v25, 0x3dd53b94, v60
	v_exp_f32_e32 v189, v18
	v_fmamk_f32 v18, v26, 0x3dd53b94, v60
	v_exp_f32_e32 v173, v18
	v_fmamk_f32 v18, v27, 0x3dd53b94, v60
	v_exp_f32_e32 v175, v18
	v_fmamk_f32 v18, v28, 0x3dd53b94, v60
	v_exp_f32_e32 v174, v18
	v_fmamk_f32 v18, v29, 0x3dd53b94, v60
	v_exp_f32_e32 v188, v18
	v_fmamk_f32 v18, v30, 0x3dd53b94, v60
	v_exp_f32_e32 v164, v18
	v_fmamk_f32 v18, v31, 0x3dd53b94, v60
	v_pk_fma_f32 v[148:149], v[48:49], s[56:57], v[60:61] op_sel_hi:[1,0,0]
	v_pk_fma_f32 v[154:155], v[46:47], s[56:57], v[60:61] op_sel_hi:[1,0,0]
	v_pk_fma_f32 v[158:159], v[44:45], s[56:57], v[60:61] op_sel_hi:[1,0,0]
	v_pk_fma_f32 v[150:151], v[42:43], s[56:57], v[60:61] op_sel_hi:[1,0,0]
	v_pk_fma_f32 v[152:153], v[40:41], s[56:57], v[60:61] op_sel_hi:[1,0,0]
	v_pk_fma_f32 v[156:157], v[38:39], s[56:57], v[60:61] op_sel_hi:[1,0,0]
	v_pk_fma_f32 v[160:161], v[36:37], s[56:57], v[60:61] op_sel_hi:[1,0,0]
	v_pk_fma_f32 v[162:163], v[34:35], s[56:57], v[60:61] op_sel_hi:[1,0,0]
	v_exp_f32_e32 v166, v18
	v_fmamk_f32 v18, v32, 0x3dd53b94, v60
	v_fmac_f32_e32 v60, 0x3dd53b94, v33
	v_exp_f32_e32 v165, v18
	v_exp_f32_e32 v167, v60
	s_addk_i32 s4, 0x4000
	v_lshl_add_u64 v[18:19], s[18:19], 0, v[50:51]
	v_add_u32_e32 v198, s4, v59
	v_lshl_add_u64 v[184:185], v[18:19], 0, v[54:55]
	v_lshl_add_u64 v[186:187], v[18:19], 0, v[52:53]
	v_mov_b64_e32 v[64:65], v[16:17]
	v_mov_b64_e32 v[48:49], v[16:17]
	v_mov_b64_e32 v[32:33], v[16:17]
	v_mov_b64_e32 v[62:63], v[14:15]
	v_mov_b64_e32 v[60:61], v[12:13]
	v_mov_b64_e32 v[58:59], v[10:11]
	v_mov_b64_e32 v[56:57], v[8:9]
	v_mov_b64_e32 v[54:55], v[6:7]
	v_mov_b64_e32 v[52:53], v[4:5]
	v_mov_b64_e32 v[50:51], v[2:3]
	v_mov_b64_e32 v[46:47], v[14:15]
	v_mov_b64_e32 v[44:45], v[12:13]
	v_mov_b64_e32 v[42:43], v[10:11]
	v_mov_b64_e32 v[40:41], v[8:9]
	v_mov_b64_e32 v[38:39], v[6:7]
	v_mov_b64_e32 v[36:37], v[4:5]
	v_mov_b64_e32 v[34:35], v[2:3]
	v_mov_b64_e32 v[30:31], v[14:15]
	v_mov_b64_e32 v[28:29], v[12:13]
	v_mov_b64_e32 v[26:27], v[10:11]
	v_mov_b64_e32 v[24:25], v[8:9]
	v_mov_b64_e32 v[22:23], v[6:7]
	v_mov_b64_e32 v[20:21], v[4:5]
	v_mov_b64_e32 v[18:19], v[2:3]
	v_and_b32_e32 v230, 63, v0
	v_lshrrev_b32_e32 v231, 6, v0
	v_lshrrev_b32_e32 v232, 4, v0
	v_mul_u32_u24_e32 v232, 0xe00, v232
	v_and_b32_e32 v233, 15, v0
	v_lshl_add_u32 v232, v233, 4, v232
	v_sub_u32_e32 v232, v186, v232
	v_lshrrev_b32_e32 v233, 3, v0
	v_and_b32_e32 v236, 7, v0
	v_lshlrev_b32_e32 v236, 4, v236
	v_lshl_add_u32 v233, v233, 7, v236
	v_sub_u32_e32 v233, v182, v233
	v_add_u32_e32 v232, 0x39d1dc00, v232
	v_add_u32_e32 v233, 0x39b15600, v233
	v_mov_b32_e32 v243, 0
	v_mov_b32_e32 v244, 0x2000
	v_mov_b32_e32 v245, 0x38000
	v_bfe_u32 v236, v230, 2, 3
	v_lshl_add_u32 v236, v231, 3, v236
	v_and_b32_e32 v237, 0xfffffff3, v236
	v_and_b32_e32 v238, 4, v236
	v_lshl_or_b32 v237, v238, 1, v237
	v_and_b32_e32 v238, 8, v236
	v_lshrrev_b32_e32 v238, 1, v238
	v_or_b32_e32 v237, v237, v238
	v_add_u32_e32 v237, 64, v237
	v_mul_u32_u24_e32 v237, 0xe00, v237
	v_add_u32_e32 v237, v237, v232
	v_lshrrev_b32_e32 v238, 5, v230
	v_lshlrev_b32_e32 v238, 6, v238
	v_and_b32_e32 v239, 3, v230
	v_lshl_add_u32 v238, v239, 4, v238
	v_add_u32_e32 v237, v237, v238
	v_add_u32_e32 v242, 0x100, v237
	v_lshl_add_u64 v[206:207], s[14:15], 0, v[242:243]
	v_mov_b32_e32 v236, v230
	v_mul_u32_u24_e32 v237, 0x2ab, v236
	v_lshrrev_b32_e32 v237, 14, v237
	v_mul_u32_u24_e32 v238, 24, v237
	v_sub_u32_e32 v238, v236, v238
	v_lshl_add_u32 v237, v231, 3, v237
	v_bfe_u32 v239, v237, 1, 3
	v_xor_b32_e32 v238, v238, v239
	v_add_u32_e32 v237, 0x80, v237
	v_mul_u32_u24_e32 v240, 0xe00, v237
	v_add_u32_e32 v240, v240, v232
	v_lshl_add_u32 v240, v238, 4, v240
	v_lshl_add_u32 v241, v237, 7, v233
	v_lshl_add_u32 v241, v238, 4, v241
	v_subrev_u32_e32 v241, 0x100, v241
	v_cmp_gt_u32_e32 vcc, 16, v238
	s_nop 1
	v_cndmask_b32_e32 v242, v241, v240, vcc
	v_cndmask_b32_e32 v205, v244, v245, vcc
	v_lshl_add_u64 v[182:183], s[14:15], 0, v[242:243]
	v_add_u32_e32 v236, 0x40, v230
	v_mul_u32_u24_e32 v237, 0x2ab, v236
	v_lshrrev_b32_e32 v237, 14, v237
	v_mul_u32_u24_e32 v238, 24, v237
	v_sub_u32_e32 v238, v236, v238
	v_lshl_add_u32 v237, v231, 3, v237
	v_bfe_u32 v239, v237, 1, 3
	v_xor_b32_e32 v238, v238, v239
	v_add_u32_e32 v237, 0x80, v237
	v_mul_u32_u24_e32 v240, 0xe00, v237
	v_add_u32_e32 v240, v240, v232
	v_lshl_add_u32 v240, v238, 4, v240
	v_lshl_add_u32 v241, v237, 7, v233
	v_lshl_add_u32 v241, v238, 4, v241
	v_subrev_u32_e32 v241, 0x100, v241
	v_cmp_gt_u32_e32 vcc, 16, v238
	s_nop 1
	v_cndmask_b32_e32 v242, v241, v240, vcc
	v_cndmask_b32_e32 v208, v244, v245, vcc
	v_lshl_add_u64 v[184:185], s[14:15], 0, v[242:243]
	v_add_u32_e32 v236, 0x80, v230
	v_mul_u32_u24_e32 v237, 0x2ab, v236
	v_lshrrev_b32_e32 v237, 14, v237
	v_mul_u32_u24_e32 v238, 24, v237
	v_sub_u32_e32 v238, v236, v238
	v_lshl_add_u32 v237, v231, 3, v237
	v_bfe_u32 v239, v237, 1, 3
	v_xor_b32_e32 v238, v238, v239
	v_add_u32_e32 v237, 0x80, v237
	v_mul_u32_u24_e32 v240, 0xe00, v237
	v_add_u32_e32 v240, v240, v232
	v_lshl_add_u32 v240, v238, 4, v240
	v_lshl_add_u32 v241, v237, 7, v233
	v_lshl_add_u32 v241, v238, 4, v241
	v_subrev_u32_e32 v241, 0x100, v241
	v_cmp_gt_u32_e32 vcc, 16, v238
	s_nop 1
	v_cndmask_b32_e32 v242, v241, v240, vcc
	v_cndmask_b32_e32 v209, v244, v245, vcc
	v_lshl_add_u64 v[186:187], s[14:15], 0, v[242:243]
.LBB0_1344:
	ds_read_b128 v[230:233], v203 offset:24576
	ds_read_b128 v[236:239], v203 offset:36864
	ds_read_b128 v[240:243], v204 offset:24576
	ds_read_b128 v[244:247], v204 offset:36864
	ds_read_b128 v[66:69], v201 offset:36864
	ds_read_b128 v[70:73], v201 offset:24576
	ds_read_b128 v[212:215], v202 offset:24576
	ds_read_b128 v[216:219], v202 offset:36864
	v_add_f32_e32 v168, 0, v169
	v_add_f32_e32 v168, v191, v168
	v_add_f32_e32 v168, v170, v168
	s_waitcnt lgkmcnt(2)
	v_mfma_f32_32x32x16_bf16 v[82:97], v[70:73], v[128:131], 0
	v_add_f32_e32 v168, v192, v168
	v_add_f32_e32 v168, v190, v168
	v_add_f32_e32 v168, v193, v168
	v_add_f32_e32 v168, v171, v168
	v_add_f32_e32 v168, v189, v168
	v_add_f32_e32 v168, v173, v168
	v_add_f32_e32 v168, v175, v168
	v_mfma_f32_32x32x16_bf16 v[66:81], v[66:69], v[128:131], 0
	v_add_f32_e32 v168, v174, v168
	v_add_f32_e32 v168, v188, v168
	v_exp_f32_e32 v162, v162
	v_add_f32_e32 v168, v164, v168
	v_exp_f32_e32 v163, v163
	v_add_f32_e32 v168, v166, v168
	v_exp_f32_e32 v160, v160
	v_mfma_f32_32x32x16_bf16 v[82:97], v[230:233], v[124:127], v[82:97]
	v_add_f32_e32 v168, v165, v168
	v_exp_f32_e32 v161, v161
	v_add_f32_e32 v168, v167, v168
	v_exp_f32_e32 v156, v156
	v_add_f32_e32 v168, v162, v168
	v_exp_f32_e32 v157, v157
	v_add_f32_e32 v168, v163, v168
	v_mfma_f32_32x32x16_bf16 v[66:81], v[236:239], v[124:127], v[66:81]
	ds_read_b128 v[230:233], v201 offset:24704
	ds_read_b128 v[236:239], v201 offset:36992
	v_exp_f32_e32 v152, v152
	v_add_f32_e32 v168, v160, v168
	v_exp_f32_e32 v153, v153
	v_add_f32_e32 v168, v161, v168
	v_exp_f32_e32 v150, v150
	v_add_f32_e32 v168, v156, v168
	v_mfma_f32_32x32x16_bf16 v[82:97], v[240:243], v[120:123], v[82:97]
	v_exp_f32_e32 v151, v151
	v_add_f32_e32 v168, v157, v168
	v_exp_f32_e32 v158, v158
	v_add_f32_e32 v168, v152, v168
	v_exp_f32_e32 v159, v159
	v_add_f32_e32 v168, v153, v168
	v_exp_f32_e32 v154, v154
	v_mfma_f32_32x32x16_bf16 v[66:81], v[244:247], v[120:123], v[66:81]
	ds_read_b128 v[240:243], v203 offset:24704
	ds_read_b128 v[244:247], v203 offset:36992
	v_add_f32_e32 v168, v150, v168
	v_exp_f32_e32 v155, v155
	v_add_f32_e32 v168, v151, v168
	v_exp_f32_e32 v148, v148
	v_add_f32_e32 v168, v158, v168
	v_exp_f32_e32 v149, v149
	s_waitcnt lgkmcnt(5)
	v_mfma_f32_32x32x16_bf16 v[82:97], v[212:215], v[116:119], v[82:97]
	v_add_f32_e32 v168, v159, v168
	v_add_f32_e32 v168, v154, v168
	v_add_f32_e32 v168, v155, v168
	v_add_f32_e32 v168, v148, v168
	s_waitcnt lgkmcnt(4)
	v_mfma_f32_32x32x16_bf16 v[66:81], v[216:219], v[116:119], v[66:81]
	ds_read_b128 v[212:215], v204 offset:24704
	ds_read_b128 v[216:219], v204 offset:36992
	s_waitcnt lgkmcnt(5)
	v_mfma_f32_32x32x16_bf16 v[82:97], v[230:233], v[112:115], v[82:97]
	s_waitcnt lgkmcnt(4)
	v_mfma_f32_32x32x16_bf16 v[66:81], v[236:239], v[112:115], v[66:81]
	ds_read_b128 v[230:233], v202 offset:24704
	ds_read_b128 v[236:239], v202 offset:36992
	s_waitcnt lgkmcnt(5)
	v_mfma_f32_32x32x16_bf16 v[82:97], v[240:243], v[108:111], v[82:97]
	s_waitcnt lgkmcnt(4)
	v_mfma_f32_32x32x16_bf16 v[66:81], v[244:247], v[108:111], v[66:81]
	ds_read_b128 v[240:243], v201 offset:24832
	ds_read_b128 v[244:247], v201 offset:37120
	s_waitcnt lgkmcnt(5)
	v_mfma_f32_32x32x16_bf16 v[82:97], v[212:215], v[104:107], v[82:97]
	s_waitcnt lgkmcnt(4)
	v_mfma_f32_32x32x16_bf16 v[66:81], v[216:219], v[104:107], v[66:81]
	ds_read_b128 v[212:215], v203 offset:24832
	ds_read_b128 v[216:219], v203 offset:37120
	s_waitcnt lgkmcnt(5)
	v_mfma_f32_32x32x16_bf16 v[82:97], v[230:233], v[100:103], v[82:97]
	s_waitcnt lgkmcnt(4)
	v_mfma_f32_32x32x16_bf16 v[66:81], v[236:239], v[100:103], v[66:81]
	ds_read_b128 v[230:233], v204 offset:24832
	ds_read_b128 v[236:239], v204 offset:37120
	s_waitcnt lgkmcnt(5)
	v_mfma_f32_32x32x16_bf16 v[82:97], v[240:243], v[144:147], v[82:97]
	s_waitcnt lgkmcnt(4)
	v_mfma_f32_32x32x16_bf16 v[66:81], v[244:247], v[144:147], v[66:81]
	ds_read_b128 v[240:243], v202 offset:24832
	ds_read_b128 v[244:247], v202 offset:37120
	s_waitcnt lgkmcnt(5)
	v_mfma_f32_32x32x16_bf16 v[82:97], v[212:215], v[140:143], v[82:97]
	v_add_f32_e32 v212, v149, v168
	v_mov_b32_e32 v213, v212
	v_cvt_pk_bf16_f32 v168, v169, v191
	v_cvt_pk_bf16_f32 v169, v170, v192
	v_cvt_pk_bf16_f32 v170, v190, v193
	v_cvt_pk_bf16_f32 v171, v171, v189
	v_cvt_pk_bf16_f32 v172, v173, v175
	s_waitcnt lgkmcnt(4)
	v_mfma_f32_32x32x16_bf16 v[66:81], v[216:219], v[140:143], v[66:81]
	v_cvt_pk_bf16_f32 v173, v174, v188
	v_cvt_pk_bf16_f32 v174, v164, v166
	v_permlane32_swap_b32_e32 v212, v213
	v_permlane32_swap_b32_e32 v168, v170
	v_cvt_pk_bf16_f32 v175, v165, v167
	s_waitcnt lgkmcnt(3)
	v_mfma_f32_32x32x16_bf16 v[82:97], v[230:233], v[136:139], v[82:97]
	v_permlane32_swap_b32_e32 v172, v174
	v_cvt_pk_bf16_f32 v214, v162, v163
	v_cvt_pk_bf16_f32 v215, v160, v161
	v_cvt_pk_bf16_f32 v216, v156, v157
	v_cvt_pk_bf16_f32 v217, v152, v153
	v_cvt_pk_bf16_f32 v230, v150, v151
	s_waitcnt lgkmcnt(2)
	v_mfma_f32_32x32x16_bf16 v[66:81], v[236:239], v[136:139], v[66:81]
	v_cvt_pk_bf16_f32 v231, v158, v159
	v_cvt_pk_bf16_f32 v232, v154, v155
	v_cvt_pk_bf16_f32 v233, v148, v149
	v_permlane32_swap_b32_e32 v169, v171
	v_permlane32_swap_b32_e32 v173, v175
	s_waitcnt lgkmcnt(1)
	v_mfma_f32_32x32x16_bf16 v[82:97], v[240:243], v[132:135], v[82:97]
	v_permlane32_swap_b32_e32 v214, v216
	v_permlane32_swap_b32_e32 v215, v217
	v_permlane32_swap_b32_e32 v230, v232
	v_permlane32_swap_b32_e32 v231, v233
	s_waitcnt lgkmcnt(0)
	v_mfma_f32_32x32x16_bf16 v[66:81], v[244:247], v[132:135], v[66:81]
	v_readfirstlane_b32 s4, v0
	s_nop 0
	s_lshl_b32 s5, s4, 4
	s_mul_i32 s4, s5, 3
	s_add_i32 m0, s4, 0x8000
	s_nop 0
	global_load_lds_dwordx4 v[182:183], off
	s_add_i32 m0, s4, 0x8400
	s_nop 0
	global_load_lds_dwordx4 v[184:185], off
	s_add_i32 m0, s4, 0x8800
	s_nop 0
	global_load_lds_dwordx4 v[186:187], off
	s_lshl_b32 s5, s5, 1
	s_add_i32 m0, s5, 0x4000
	s_nop 0
	global_load_lds_dwordx4 v[206:207], off
	s_add_i32 m0, s5, 0x4380
	s_nop 0
	global_load_lds_dwordx4 v[206:207], off offset:128
	v_add_co_u32_e32 v182, vcc, v182, v205
	s_nop 1
	v_addc_co_u32_e32 v183, vcc, 0, v183, vcc
	v_add_co_u32_e32 v184, vcc, v184, v208
	s_nop 1
	v_addc_co_u32_e32 v185, vcc, 0, v185, vcc
	v_add_co_u32_e32 v186, vcc, v186, v209
	s_nop 1
	v_addc_co_u32_e32 v187, vcc, 0, v187, vcc
	v_add_co_u32_e32 v206, vcc, 0x38000, v206
	s_nop 1
	v_addc_co_u32_e32 v207, vcc, 0, v207, vcc
	ds_read_b64_tr_b16 v[236:237], v200 offset:0
	ds_read_b64_tr_b16 v[238:239], v200 offset:0x800
	ds_read_b64_tr_b16 v[240:241], v200 offset:0x1000
	ds_read_b64_tr_b16 v[242:243], v200 offset:0x1800
	ds_read_b64_tr_b16 v[244:245], v200 offset:0x2000
	ds_read_b64_tr_b16 v[246:247], v200 offset:0x2800
	ds_read_b64_tr_b16 v[222:223], v200 offset:0x3000
	ds_read_b64_tr_b16 v[224:225], v200 offset:0x3800
	s_waitcnt lgkmcnt(0)
	s_nop 0
	v_mfma_f32_32x32x16_bf16 v[2:17], v[168:171], v[236:239], v[2:17]
	v_mfma_f32_32x32x16_bf16 v[2:17], v[172:175], v[240:243], v[2:17]
	v_mfma_f32_32x32x16_bf16 v[2:17], v[214:217], v[244:247], v[2:17]
	v_mfma_f32_32x32x16_bf16 v[2:17], v[230:233], v[222:225], v[2:17]
	ds_read_b64_tr_b16 v[222:223], v200 offset:0x200
	ds_read_b64_tr_b16 v[224:225], v200 offset:0xa00
	ds_read_b64_tr_b16 v[236:237], v200 offset:0x1200
	ds_read_b64_tr_b16 v[238:239], v200 offset:0x1a00
	ds_read_b64_tr_b16 v[240:241], v200 offset:0x2200
	ds_read_b64_tr_b16 v[242:243], v200 offset:0x2a00
	ds_read_b64_tr_b16 v[244:245], v200 offset:0x3200
	ds_read_b64_tr_b16 v[246:247], v200 offset:0x3a00
	s_waitcnt lgkmcnt(0)
	s_nop 0
	v_mfma_f32_32x32x16_bf16 v[50:65], v[168:171], v[222:225], v[50:65]
	ds_read_b64_tr_b16 v[222:223], v200 offset:0x400
	ds_read_b64_tr_b16 v[224:225], v200 offset:0xc00
	v_mfma_f32_32x32x16_bf16 v[50:65], v[172:175], v[236:239], v[50:65]
	ds_read_b64_tr_b16 v[236:237], v200 offset:0x1400
	ds_read_b64_tr_b16 v[238:239], v200 offset:0x1c00
	v_mfma_f32_32x32x16_bf16 v[50:65], v[214:217], v[240:243], v[50:65]
	ds_read_b64_tr_b16 v[240:241], v200 offset:0x2400
	ds_read_b64_tr_b16 v[242:243], v200 offset:0x2c00
	v_mfma_f32_32x32x16_bf16 v[50:65], v[230:233], v[244:247], v[50:65]
	ds_read_b64_tr_b16 v[244:245], v200 offset:0x3400
	ds_read_b64_tr_b16 v[246:247], v200 offset:0x3c00
	s_waitcnt lgkmcnt(0)
	v_mfma_f32_32x32x16_bf16 v[34:49], v[168:171], v[222:225], v[34:49]
	ds_read_b64_tr_b16 v[222:223], v200 offset:0x600
	ds_read_b64_tr_b16 v[224:225], v200 offset:0xe00
	v_mfma_f32_32x32x16_bf16 v[34:49], v[172:175], v[236:239], v[34:49]
	ds_read_b64_tr_b16 v[236:237], v200 offset:0x1600
	ds_read_b64_tr_b16 v[238:239], v200 offset:0x1e00
	v_mfma_f32_32x32x16_bf16 v[34:49], v[214:217], v[240:243], v[34:49]
	ds_read_b64_tr_b16 v[240:241], v200 offset:0x2600
	ds_read_b64_tr_b16 v[242:243], v200 offset:0x2e00
	v_mfma_f32_32x32x16_bf16 v[34:49], v[230:233], v[244:247], v[34:49]
	ds_read_b64_tr_b16 v[244:245], v200 offset:0x3600
	ds_read_b64_tr_b16 v[246:247], v200 offset:0x3e00
	s_waitcnt lgkmcnt(0)
	v_mfma_f32_32x32x16_bf16 v[18:33], v[168:171], v[222:225], v[18:33]
	v_max_f32_e32 v168, v83, v83
	v_max_f32_e32 v169, v82, v82
	v_max_f32_e32 v168, v169, v168
	v_max3_f32 v168, v168, v84, v85
	v_max3_f32 v168, v168, v86, v87
	v_max3_f32 v168, v168, v88, v89
	v_max3_f32 v168, v168, v90, v91
	v_max3_f32 v168, v168, v92, v93
	v_max3_f32 v168, v168, v94, v95
	v_mfma_f32_32x32x16_bf16 v[18:33], v[172:175], v[236:239], v[18:33]
	v_max3_f32 v168, v168, v96, v97
	v_max3_f32 v168, v168, v66, v67
	v_max3_f32 v168, v168, v68, v69
	v_max3_f32 v168, v168, v70, v71
	v_max3_f32 v168, v168, v72, v73
	v_max3_f32 v168, v168, v74, v75
	v_max3_f32 v168, v168, v76, v77
	v_max3_f32 v168, v168, v78, v79
	v_mfma_f32_32x32x16_bf16 v[18:33], v[214:217], v[240:243], v[18:33]
	v_max3_f32 v168, v168, v80, v81
	v_mov_b32_e32 v169, v168
	s_nop 1
	v_permlane32_swap_b32_e32 v168, v169
	v_max_f32_e32 v169, v169, v169
	v_max_f32_e32 v168, v168, v168
	v_max_f32_e32 v168, v168, v169
	v_sub_f32_e32 v169, v168, v211
	v_cmp_ge_f32_e32 vcc, s11, v169
	v_max_f32_e32 v169, v211, v211
	v_max_f32_e32 v168, v169, v168
	v_mfma_f32_32x32x16_bf16 v[18:33], v[230:233], v[244:247], v[18:33]
	v_sub_f32_e32 v169, v211, v168
	v_mul_f32_e32 v169, 0x3dd53b94, v169
	v_exp_f32_e32 v169, v169
	s_cmp_eq_u64 vcc, exec
	s_cselect_b64 s[18:19], -1, 0
	v_cndmask_b32_e64 v172, v169, 1.0, s[18:19]
	v_cmp_gt_f32_e32 vcc, 1.0, v172
	s_cbranch_vccz .LBB0_1348
	s_and_saveexec_b64 s[4:5], s[0:1]
	ds_write_b32 v197, v172 offset:128
	s_or_b64 exec, exec, s[4:5]
	s_waitcnt lgkmcnt(0)
	v_add_u32_e32 v160, v196, v98
	ds_read_b128 v[148:151], v160 offset:224
	ds_read_b128 v[152:155], v160 offset:192
	ds_read_b128 v[156:159], v160 offset:160
	ds_read_b128 v[160:163], v160 offset:128
	v_mov_b32_e32 v228, 0xffffce00
	s_waitcnt lgkmcnt(3)
	v_pk_mul_f32 v[14:15], v[14:15], v[148:149]
	s_waitcnt lgkmcnt(2)
	v_pk_mul_f32 v[10:11], v[10:11], v[152:153]
	s_waitcnt lgkmcnt(1)
	v_pk_mul_f32 v[6:7], v[6:7], v[156:157]
	v_pk_mul_f32 v[16:17], v[16:17], v[150:151]
	v_pk_mul_f32 v[12:13], v[12:13], v[154:155]
	v_pk_mul_f32 v[8:9], v[8:9], v[158:159]
	s_waitcnt lgkmcnt(0)
	v_pk_mul_f32 v[4:5], v[4:5], v[162:163]
	v_pk_mul_f32 v[2:3], v[2:3], v[160:161]
	v_pk_mul_f32 v[62:63], v[62:63], v[148:149]
	v_pk_mul_f32 v[58:59], v[58:59], v[152:153]
	v_pk_mul_f32 v[54:55], v[54:55], v[156:157]
	v_pk_mul_f32 v[64:65], v[64:65], v[150:151]
	v_pk_mul_f32 v[60:61], v[60:61], v[154:155]
	v_pk_mul_f32 v[56:57], v[56:57], v[158:159]
	v_pk_mul_f32 v[52:53], v[52:53], v[162:163]
	v_pk_mul_f32 v[50:51], v[50:51], v[160:161]
	v_pk_mul_f32 v[46:47], v[46:47], v[148:149]
	v_pk_mul_f32 v[42:43], v[42:43], v[152:153]
	v_pk_mul_f32 v[38:39], v[38:39], v[156:157]
	v_pk_mul_f32 v[48:49], v[48:49], v[150:151]
	v_pk_mul_f32 v[44:45], v[44:45], v[154:155]
	v_pk_mul_f32 v[40:41], v[40:41], v[158:159]
	v_pk_mul_f32 v[36:37], v[36:37], v[162:163]
	v_pk_mul_f32 v[34:35], v[34:35], v[160:161]
	v_pk_mul_f32 v[30:31], v[30:31], v[148:149]
	v_pk_mul_f32 v[26:27], v[26:27], v[152:153]
	v_pk_mul_f32 v[22:23], v[22:23], v[156:157]
	v_pk_mul_f32 v[32:33], v[32:33], v[150:151]
	v_pk_mul_f32 v[28:29], v[28:29], v[154:155]
	v_pk_mul_f32 v[24:25], v[24:25], v[158:159]
	v_pk_mul_f32 v[20:21], v[20:21], v[162:163]
	v_pk_mul_f32 v[18:19], v[18:19], v[160:161]
	s_branch .LBB0_1349

.LBB0_1349:
	v_cndmask_b32_e64 v173, v168, v211, s[18:19]
	v_mul_f32_e32 v164, 0xbdd53b94, v173
	v_fmamk_f32 v82, v82, 0x3dd53b94, v164
	v_fmamk_f32 v83, v83, 0x3dd53b94, v164
	v_fmamk_f32 v84, v84, 0x3dd53b94, v164
	v_fmamk_f32 v85, v85, 0x3dd53b94, v164
	v_fmamk_f32 v86, v86, 0x3dd53b94, v164
	v_fmamk_f32 v87, v87, 0x3dd53b94, v164
	v_fmamk_f32 v88, v88, 0x3dd53b94, v164
	v_fmamk_f32 v89, v89, 0x3dd53b94, v164
	v_fmamk_f32 v90, v90, 0x3dd53b94, v164
	v_fmamk_f32 v91, v91, 0x3dd53b94, v164
	v_fmamk_f32 v92, v92, 0x3dd53b94, v164
	v_fmamk_f32 v93, v93, 0x3dd53b94, v164
	v_fmamk_f32 v94, v94, 0x3dd53b94, v164
	v_fmamk_f32 v95, v95, 0x3dd53b94, v164
	v_fmamk_f32 v96, v96, 0x3dd53b94, v164
	v_fmamk_f32 v97, v97, 0x3dd53b94, v164
	v_fmamk_f32 v229, v68, 0x3dd53b94, v164
	v_fmamk_f32 v230, v69, 0x3dd53b94, v164
	v_fmamk_f32 v168, v73, 0x3dd53b94, v164
	v_fmamk_f32 v169, v74, 0x3dd53b94, v164
	v_fmamk_f32 v175, v66, 0x3dd53b94, v164
	v_fmamk_f32 v211, v67, 0x3dd53b94, v164
	v_fmamk_f32 v231, v70, 0x3dd53b94, v164
	v_fmamk_f32 v166, v71, 0x3dd53b94, v164
	v_fmamk_f32 v167, v72, 0x3dd53b94, v164
	v_fmamk_f32 v170, v75, 0x3dd53b94, v164
	v_fmamk_f32 v171, v76, 0x3dd53b94, v164
	v_fmamk_f32 v174, v77, 0x3dd53b94, v164
	v_fmamk_f32 v165, v78, 0x3dd53b94, v164
	v_exp_f32_e32 v161, v82
	v_exp_f32_e32 v163, v83
	v_exp_f32_e32 v159, v84
	v_exp_f32_e32 v162, v85
	v_exp_f32_e32 v158, v86
	v_exp_f32_e32 v160, v87
	v_exp_f32_e32 v156, v88
	v_exp_f32_e32 v157, v89
	v_exp_f32_e32 v153, v90
	v_exp_f32_e32 v155, v91
	v_exp_f32_e32 v152, v92
	v_exp_f32_e32 v154, v93
	v_exp_f32_e32 v149, v94
	v_exp_f32_e32 v151, v95
	v_exp_f32_e32 v148, v96
	v_exp_f32_e32 v150, v97
	v_fmamk_f32 v232, v79, 0x3dd53b94, v164
	v_fmamk_f32 v233, v80, 0x3dd53b94, v164
	v_fmac_f32_e32 v164, 0x3dd53b94, v81
	s_waitcnt vmcnt(0) lgkmcnt(0)
	s_barrier
	ds_read_b128 v[214:217], v203
	ds_read_b128 v[222:225], v203 offset:12288
	ds_read_b128 v[236:239], v204
	ds_read_b128 v[240:243], v204 offset:12288
	ds_read_b128 v[66:69], v201 offset:12288
	ds_read_b128 v[70:73], v201
	ds_read_b128 v[244:247], v202
	ds_read_b128 v[176:179], v202 offset:12288
	v_exp_f32_e32 v166, v166
	v_exp_f32_e32 v167, v167
	v_exp_f32_e32 v218, v169
	s_waitcnt lgkmcnt(2)
	v_mfma_f32_32x32x16_bf16 v[82:97], v[70:73], v[128:131], 0
	v_exp_f32_e32 v219, v170
	v_exp_f32_e32 v165, v165
	v_exp_f32_e32 v164, v164
	v_mfma_f32_32x32x16_bf16 v[82:97], v[214:217], v[124:127], v[82:97]
	v_mfma_f32_32x32x16_bf16 v[82:97], v[236:239], v[120:123], v[82:97]
	v_mfma_f32_32x32x16_bf16 v[66:81], v[66:69], v[128:131], 0
	s_waitcnt lgkmcnt(1)
	v_mfma_f32_32x32x16_bf16 v[82:97], v[244:247], v[116:119], v[82:97]
	v_mfma_f32_32x32x16_bf16 v[66:81], v[222:225], v[124:127], v[66:81]
	ds_read_b128 v[214:217], v201 offset:128
	ds_read_b128 v[222:225], v201 offset:12416
	s_waitcnt lgkmcnt(1)
	v_mfma_f32_32x32x16_bf16 v[82:97], v[214:217], v[112:115], v[82:97]
	v_mfma_f32_32x32x16_bf16 v[66:81], v[240:243], v[120:123], v[66:81]
	ds_read_b128 v[236:239], v203 offset:128
	ds_read_b128 v[240:243], v203 offset:12416
	s_waitcnt lgkmcnt(1)
	v_mfma_f32_32x32x16_bf16 v[82:97], v[236:239], v[108:111], v[82:97]
	v_mfma_f32_32x32x16_bf16 v[66:81], v[176:179], v[116:119], v[66:81]
	ds_read_b128 v[176:179], v204 offset:128
	ds_read_b128 v[244:247], v204 offset:12416
	s_waitcnt lgkmcnt(1)
	v_mfma_f32_32x32x16_bf16 v[82:97], v[176:179], v[104:107], v[82:97]
	v_mfma_f32_32x32x16_bf16 v[66:81], v[222:225], v[112:115], v[66:81]
	ds_read_b128 v[214:217], v202 offset:128
	ds_read_b128 v[222:225], v202 offset:12416
	s_waitcnt lgkmcnt(1)
	v_mfma_f32_32x32x16_bf16 v[82:97], v[214:217], v[100:103], v[82:97]
	v_mfma_f32_32x32x16_bf16 v[66:81], v[240:243], v[108:111], v[66:81]
	ds_read_b128 v[236:239], v201 offset:256
	ds_read_b128 v[240:243], v201 offset:12544
	s_waitcnt lgkmcnt(1)
	v_mfma_f32_32x32x16_bf16 v[82:97], v[236:239], v[144:147], v[82:97]
	v_mfma_f32_32x32x16_bf16 v[66:81], v[244:247], v[104:107], v[66:81]
	ds_read_b128 v[176:179], v203 offset:256
	ds_read_b128 v[244:247], v203 offset:12544
	s_waitcnt lgkmcnt(1)
	v_mfma_f32_32x32x16_bf16 v[82:97], v[176:179], v[140:143], v[82:97]
	v_exp_f32_e32 v178, v175
	v_exp_f32_e32 v179, v211
	v_exp_f32_e32 v211, v229
	v_mfma_f32_32x32x16_bf16 v[66:81], v[222:225], v[100:103], v[66:81]
	ds_read_b128 v[214:217], v204 offset:256
	ds_read_b128 v[222:225], v204 offset:12544
	s_waitcnt lgkmcnt(1)
	v_mfma_f32_32x32x16_bf16 v[82:97], v[214:217], v[136:139], v[82:97]
	v_exp_f32_e32 v217, v168
	v_add_f32_e32 v168, 0, v161
	v_add_f32_e32 v168, v163, v168
	v_add_f32_e32 v168, v159, v168
	v_add_f32_e32 v168, v162, v168
	v_add_f32_e32 v168, v158, v168
	v_add_f32_e32 v168, v160, v168
	v_mfma_f32_32x32x16_bf16 v[66:81], v[240:243], v[144:147], v[66:81]
	v_add_f32_e32 v168, v156, v168
	v_add_f32_e32 v168, v157, v168
	v_add_f32_e32 v168, v153, v168
	v_add_f32_e32 v168, v155, v168
	v_add_f32_e32 v168, v152, v168
	v_add_f32_e32 v168, v154, v168
	v_add_f32_e32 v168, v149, v168
	v_mfma_f32_32x32x16_bf16 v[66:81], v[244:247], v[140:143], v[66:81]
	v_add_f32_e32 v168, v151, v168
	v_add_f32_e32 v168, v148, v168
	v_exp_f32_e32 v215, v230
	v_add_f32_e32 v168, v150, v168
	v_exp_f32_e32 v216, v231
	v_add_f32_e32 v168, v178, v168
	v_add_f32_e32 v168, v179, v168
	s_waitcnt lgkmcnt(0)
	v_mfma_f32_32x32x16_bf16 v[66:81], v[222:225], v[136:139], v[66:81]
	v_add_f32_e32 v168, v211, v168
	v_add_f32_e32 v168, v215, v168
	v_add_f32_e32 v168, v216, v168
	ds_read_b128 v[236:239], v202 offset:256
	ds_read_b128 v[240:243], v202 offset:12544
	v_add_f32_e32 v168, v166, v168
	v_exp_f32_e32 v223, v171
	v_add_f32_e32 v168, v167, v168
	v_exp_f32_e32 v224, v174
	v_add_f32_e32 v168, v217, v168
	v_add_f32_e32 v168, v218, v168
	v_exp_f32_e32 v225, v232
	v_add_f32_e32 v168, v219, v168
	s_waitcnt lgkmcnt(1)
	v_mfma_f32_32x32x16_bf16 v[82:97], v[236:239], v[132:135], v[82:97]
	v_exp_f32_e32 v231, v233
	v_add_f32_e32 v168, v223, v168
	v_add_f32_e32 v168, v224, v168
	v_add_f32_e32 v168, v165, v168
	v_add_f32_e32 v168, v225, v168
	v_add_f32_e32 v168, v231, v168
	v_add_f32_e32 v229, v164, v168
	s_waitcnt lgkmcnt(0)
	v_mfma_f32_32x32x16_bf16 v[66:81], v[240:243], v[132:135], v[66:81]
	v_mov_b32_e32 v230, v229
	v_cvt_pk_bf16_f32 v168, v161, v163
	v_cvt_pk_bf16_f32 v169, v159, v162
	v_cvt_pk_bf16_f32 v170, v158, v160
	v_cvt_pk_bf16_f32 v171, v156, v157
	s_nop 1
	v_permlane32_swap_b32_e32 v229, v230
	v_permlane32_swap_b32_e32 v168, v170
	v_permlane32_swap_b32_e32 v169, v171
	v_cvt_pk_bf16_f32 v174, v153, v155
	v_cvt_pk_bf16_f32 v175, v152, v154
	v_cvt_pk_bf16_f32 v176, v149, v151
	v_cvt_pk_bf16_f32 v177, v148, v150
	v_cvt_pk_bf16_f32 v214, v178, v179
	v_cvt_pk_bf16_f32 v215, v211, v215
	v_cvt_pk_bf16_f32 v216, v216, v166
	v_cvt_pk_bf16_f32 v217, v167, v217
	v_cvt_pk_bf16_f32 v222, v218, v219
	v_cvt_pk_bf16_f32 v223, v223, v224
	v_cvt_pk_bf16_f32 v224, v165, v225
	v_cvt_pk_bf16_f32 v225, v231, v164
	s_nop 0
	v_permlane32_swap_b32_e32 v174, v176
	v_permlane32_swap_b32_e32 v175, v177
	v_permlane32_swap_b32_e32 v214, v216
	v_permlane32_swap_b32_e32 v215, v217
	v_permlane32_swap_b32_e32 v222, v224
	v_permlane32_swap_b32_e32 v223, v225
	v_readfirstlane_b32 s4, v0
	s_nop 0
	s_lshl_b32 s5, s4, 4
	s_mul_i32 s4, s5, 3
	s_add_i32 m0, s4, 0xe000
	s_nop 0
	global_load_lds_dwordx4 v[182:183], off
	s_add_i32 m0, s4, 0xe400
	s_nop 0
	global_load_lds_dwordx4 v[184:185], off
	s_add_i32 m0, s4, 0xe800
	s_nop 0
	global_load_lds_dwordx4 v[186:187], off
	s_lshl_b32 s5, s5, 1
	s_mov_b32 m0, s5
	s_nop 0
	global_load_lds_dwordx4 v[206:207], off
	s_add_i32 m0, s5, 0x380
	s_nop 0
	global_load_lds_dwordx4 v[206:207], off offset:128
	v_add_co_u32_e32 v182, vcc, v182, v205
	s_nop 1
	v_addc_co_u32_e32 v183, vcc, 0, v183, vcc
	v_add_co_u32_e32 v184, vcc, v184, v208
	s_nop 1
	v_addc_co_u32_e32 v185, vcc, 0, v185, vcc
	v_add_co_u32_e32 v186, vcc, v186, v209
	s_nop 1
	v_addc_co_u32_e32 v187, vcc, 0, v187, vcc
	v_add_co_u32_e32 v206, vcc, 0x38000, v206
	s_nop 1
	v_addc_co_u32_e32 v207, vcc, 0, v207, vcc
	ds_read_b64_tr_b16 v[188:189], v198 offset:0
	ds_read_b64_tr_b16 v[190:191], v198 offset:0x800
	ds_read_b64_tr_b16 v[236:237], v198 offset:0x1000
	ds_read_b64_tr_b16 v[238:239], v198 offset:0x1800
	ds_read_b64_tr_b16 v[240:241], v198 offset:0x2000
	ds_read_b64_tr_b16 v[242:243], v198 offset:0x2800
	ds_read_b64_tr_b16 v[244:245], v198 offset:0x3000
	ds_read_b64_tr_b16 v[246:247], v198 offset:0x3800
	s_waitcnt lgkmcnt(0)
	s_nop 0
	v_mfma_f32_32x32x16_bf16 v[2:17], v[168:171], v[188:191], v[2:17]
	ds_read_b64_tr_b16 v[188:189], v198 offset:0x200
	ds_read_b64_tr_b16 v[190:191], v198 offset:0xa00
	v_mfma_f32_32x32x16_bf16 v[2:17], v[174:177], v[236:239], v[2:17]
	ds_read_b64_tr_b16 v[236:237], v198 offset:0x1200
	ds_read_b64_tr_b16 v[238:239], v198 offset:0x1a00
	v_mfma_f32_32x32x16_bf16 v[2:17], v[214:217], v[240:243], v[2:17]
	ds_read_b64_tr_b16 v[240:241], v198 offset:0x2200
	ds_read_b64_tr_b16 v[242:243], v198 offset:0x2a00
	v_mfma_f32_32x32x16_bf16 v[2:17], v[222:225], v[244:247], v[2:17]
	ds_read_b64_tr_b16 v[244:245], v198 offset:0x3200
	ds_read_b64_tr_b16 v[246:247], v198 offset:0x3a00
	s_waitcnt lgkmcnt(0)
	v_mfma_f32_32x32x16_bf16 v[50:65], v[168:171], v[188:191], v[50:65]
	ds_read_b64_tr_b16 v[188:189], v198 offset:0x400
	ds_read_b64_tr_b16 v[190:191], v198 offset:0xc00
	v_mfma_f32_32x32x16_bf16 v[50:65], v[174:177], v[236:239], v[50:65]
	ds_read_b64_tr_b16 v[236:237], v198 offset:0x1400
	ds_read_b64_tr_b16 v[238:239], v198 offset:0x1c00
	v_mfma_f32_32x32x16_bf16 v[50:65], v[214:217], v[240:243], v[50:65]
	ds_read_b64_tr_b16 v[240:241], v198 offset:0x2400
	ds_read_b64_tr_b16 v[242:243], v198 offset:0x2c00
	v_mfma_f32_32x32x16_bf16 v[50:65], v[222:225], v[244:247], v[50:65]
	ds_read_b64_tr_b16 v[244:245], v198 offset:0x3400
	ds_read_b64_tr_b16 v[246:247], v198 offset:0x3c00
	s_waitcnt lgkmcnt(0)
	v_mfma_f32_32x32x16_bf16 v[34:49], v[168:171], v[188:191], v[34:49]
	ds_read_b64_tr_b16 v[188:189], v198 offset:0x600
	ds_read_b64_tr_b16 v[190:191], v198 offset:0xe00
	v_mfma_f32_32x32x16_bf16 v[34:49], v[174:177], v[236:239], v[34:49]
	ds_read_b64_tr_b16 v[236:237], v198 offset:0x1600
	ds_read_b64_tr_b16 v[238:239], v198 offset:0x1e00
	v_mfma_f32_32x32x16_bf16 v[34:49], v[214:217], v[240:243], v[34:49]
	ds_read_b64_tr_b16 v[240:241], v198 offset:0x2600
	ds_read_b64_tr_b16 v[242:243], v198 offset:0x2e00
	v_mfma_f32_32x32x16_bf16 v[34:49], v[222:225], v[244:247], v[34:49]
	ds_read_b64_tr_b16 v[244:245], v198 offset:0x3600
	ds_read_b64_tr_b16 v[246:247], v198 offset:0x3e00
	s_waitcnt lgkmcnt(0)
	v_mfma_f32_32x32x16_bf16 v[18:33], v[168:171], v[188:191], v[18:33]
	v_max_f32_e32 v168, v83, v83
	v_max_f32_e32 v169, v82, v82
	v_max_f32_e32 v168, v169, v168
	v_max3_f32 v168, v168, v84, v85
	v_max3_f32 v168, v168, v86, v87
	v_max3_f32 v168, v168, v88, v89
	v_max3_f32 v168, v168, v90, v91
	v_max3_f32 v168, v168, v92, v93
	v_max3_f32 v168, v168, v94, v95
	v_mfma_f32_32x32x16_bf16 v[18:33], v[174:177], v[236:239], v[18:33]
	v_max3_f32 v168, v168, v96, v97
	v_max3_f32 v168, v168, v66, v67
	v_max3_f32 v168, v168, v68, v69
	v_max3_f32 v168, v168, v70, v71
	v_max3_f32 v168, v168, v72, v73
	v_max3_f32 v168, v168, v74, v75
	v_max3_f32 v168, v168, v76, v77
	v_max3_f32 v168, v168, v78, v79
	v_mfma_f32_32x32x16_bf16 v[18:33], v[214:217], v[240:243], v[18:33]
	v_max3_f32 v168, v168, v80, v81
	v_mov_b32_e32 v169, v168
	s_nop 1
	v_permlane32_swap_b32_e32 v168, v169
	v_max_f32_e32 v169, v169, v169
	v_max_f32_e32 v168, v168, v168
	v_max_f32_e32 v168, v168, v169
	v_sub_f32_e32 v169, v168, v173
	v_cmp_ge_f32_e32 vcc, s11, v169
	v_max_f32_e32 v169, v173, v173
	v_max_f32_e32 v169, v169, v168
	v_mfma_f32_32x32x16_bf16 v[18:33], v[222:225], v[244:247], v[18:33]
	v_sub_f32_e32 v168, v173, v169
	v_mul_f32_e32 v168, 0x3dd53b94, v168
	v_exp_f32_e32 v168, v168
	s_cmp_eq_u64 vcc, exec
	s_cselect_b64 s[18:19], -1, 0
	v_cndmask_b32_e64 v168, v168, 1.0, s[18:19]
	v_cmp_gt_f32_e32 vcc, 1.0, v168
	s_cbranch_vccz .LBB0_1353
	s_mov_b64 s[4:5], exec
	s_and_b64 s[22:23], s[4:5], s[0:1]
	v_mov_b32_e32 v246, v227
	s_mov_b64 exec, s[22:23]
	ds_write_b32 v197, v168 offset:128
	s_or_b64 exec, exec, s[4:5]
	s_waitcnt lgkmcnt(0)
	v_add_u32_e32 v160, v196, v98
	ds_read_b128 v[148:151], v160 offset:224
	ds_read_b128 v[152:155], v160 offset:192
	ds_read_b128 v[156:159], v160 offset:160
	ds_read_b128 v[160:163], v160 offset:128
	s_waitcnt lgkmcnt(3)
	v_pk_mul_f32 v[14:15], v[14:15], v[148:149]
	s_waitcnt lgkmcnt(2)
	v_pk_mul_f32 v[10:11], v[10:11], v[152:153]
	s_waitcnt lgkmcnt(1)
	v_pk_mul_f32 v[6:7], v[6:7], v[156:157]
	v_pk_mul_f32 v[16:17], v[16:17], v[150:151]
	v_pk_mul_f32 v[12:13], v[12:13], v[154:155]
	v_pk_mul_f32 v[8:9], v[8:9], v[158:159]
	s_waitcnt lgkmcnt(0)
	v_pk_mul_f32 v[4:5], v[4:5], v[162:163]
	v_pk_mul_f32 v[2:3], v[2:3], v[160:161]
	v_pk_mul_f32 v[62:63], v[62:63], v[148:149]
	v_pk_mul_f32 v[58:59], v[58:59], v[152:153]
	v_pk_mul_f32 v[54:55], v[54:55], v[156:157]
	v_pk_mul_f32 v[64:65], v[64:65], v[150:151]
	v_pk_mul_f32 v[60:61], v[60:61], v[154:155]
	v_pk_mul_f32 v[56:57], v[56:57], v[158:159]
	v_pk_mul_f32 v[52:53], v[52:53], v[162:163]
	v_pk_mul_f32 v[50:51], v[50:51], v[160:161]
	v_pk_mul_f32 v[46:47], v[46:47], v[148:149]
	v_pk_mul_f32 v[42:43], v[42:43], v[152:153]
	v_pk_mul_f32 v[38:39], v[38:39], v[156:157]
	v_pk_mul_f32 v[48:49], v[48:49], v[150:151]
	v_pk_mul_f32 v[44:45], v[44:45], v[154:155]
	v_pk_mul_f32 v[40:41], v[40:41], v[158:159]
	v_pk_mul_f32 v[36:37], v[36:37], v[162:163]
	v_pk_mul_f32 v[34:35], v[34:35], v[160:161]
	v_pk_mul_f32 v[30:31], v[30:31], v[148:149]
	v_pk_mul_f32 v[26:27], v[26:27], v[152:153]
	v_pk_mul_f32 v[22:23], v[22:23], v[156:157]
	v_pk_mul_f32 v[32:33], v[32:33], v[150:151]
	v_pk_mul_f32 v[28:29], v[28:29], v[154:155]
	v_pk_mul_f32 v[24:25], v[24:25], v[158:159]
	v_pk_mul_f32 v[20:21], v[20:21], v[162:163]
	v_pk_mul_f32 v[18:19], v[18:19], v[160:161]
	s_branch .LBB0_1354

.LBB0_1354:
	v_cndmask_b32_e64 v211, v169, v173, s[18:19]
	v_mul_f32_e32 v148, 0xbdd53b94, v211
	v_mov_b32_e32 v149, v148
	v_fmamk_f32 v82, v82, 0x3dd53b94, v148
	v_fmamk_f32 v83, v83, 0x3dd53b94, v148
	v_fmamk_f32 v84, v84, 0x3dd53b94, v148
	v_fmamk_f32 v85, v85, 0x3dd53b94, v148
	v_fmamk_f32 v86, v86, 0x3dd53b94, v148
	v_fmamk_f32 v87, v87, 0x3dd53b94, v148
	v_fmamk_f32 v88, v88, 0x3dd53b94, v148
	v_fmamk_f32 v89, v89, 0x3dd53b94, v148
	v_fmamk_f32 v90, v90, 0x3dd53b94, v148
	v_fmamk_f32 v91, v91, 0x3dd53b94, v148
	v_fmamk_f32 v92, v92, 0x3dd53b94, v148
	v_fmamk_f32 v93, v93, 0x3dd53b94, v148
	v_fmamk_f32 v94, v94, 0x3dd53b94, v148
	v_fmamk_f32 v95, v95, 0x3dd53b94, v148
	v_fmamk_f32 v96, v96, 0x3dd53b94, v148
	v_fmac_f32_e32 v149, 0x3dd53b94, v97
	v_exp_f32_e32 v169, v82
	v_exp_f32_e32 v191, v83
	v_exp_f32_e32 v170, v84
	v_exp_f32_e32 v192, v85
	v_exp_f32_e32 v190, v86
	v_exp_f32_e32 v193, v87
	v_exp_f32_e32 v171, v88
	v_exp_f32_e32 v189, v89
	v_exp_f32_e32 v173, v90
	v_exp_f32_e32 v175, v91
	v_exp_f32_e32 v174, v92
	v_exp_f32_e32 v188, v93
	v_exp_f32_e32 v164, v94
	v_exp_f32_e32 v166, v95
	v_exp_f32_e32 v165, v96
	v_exp_f32_e32 v167, v149
	v_pk_fma_f32 v[162:163], v[66:67], s[56:57], v[148:149] op_sel_hi:[1,0,0]
	v_add_f32_e32 v66, v212, v213
	v_fmac_f32_e32 v66, v210, v199
	v_add_f32_e32 v199, v229, v230
	s_add_i32 s8, s8, 2
	v_pk_fma_f32 v[160:161], v[68:69], s[56:57], v[148:149] op_sel_hi:[1,0,0]
	v_pk_fma_f32 v[156:157], v[70:71], s[56:57], v[148:149] op_sel_hi:[1,0,0]
	v_pk_fma_f32 v[152:153], v[72:73], s[56:57], v[148:149] op_sel_hi:[1,0,0]
	v_pk_fma_f32 v[150:151], v[74:75], s[56:57], v[148:149] op_sel_hi:[1,0,0]
	v_pk_fma_f32 v[158:159], v[76:77], s[56:57], v[148:149] op_sel_hi:[1,0,0]
	v_pk_fma_f32 v[154:155], v[78:79], s[56:57], v[148:149] op_sel_hi:[1,0,0]
	v_pk_fma_f32 v[148:149], v[80:81], s[56:57], v[148:149] op_sel_hi:[1,0,0]
	v_fmac_f32_e32 v199, v66, v172
	s_cmp_ge_u32 s8, s3
	s_waitcnt vmcnt(0) lgkmcnt(0)
	s_barrier
	s_cbranch_scc1 .LBB0_1356
	v_mov_b32_e32 v227, 0x3200
	v_mov_b32_e32 v210, v168
	s_branch .LBB0_1344
.LBB0_1356:
	v_readfirstlane_b32 s4, v0
	s_nop 0
	s_lshl_b32 s5, s4, 4
	s_lshl_b32 s5, s5, 1
	s_add_i32 m0, s5, 0x4000
	s_nop 0
	global_load_lds_dwordx4 v[206:207], off
	s_add_i32 m0, s5, 0x4380
	s_nop 0
	global_load_lds_dwordx4 v[206:207], off offset:128
	ds_read_b128 v[182:185], v203 offset:24576
	ds_read_b128 v[206:209], v203 offset:36864
	ds_read_b128 v[230:233], v204 offset:24576
	ds_read_b128 v[236:239], v204 offset:36864
	ds_read_b128 v[66:69], v201 offset:36864
	ds_read_b128 v[70:73], v201 offset:24576
	s_waitcnt lgkmcnt(0)
	v_mfma_f32_32x32x16_bf16 v[82:97], v[70:73], v[128:131], 0
	v_mfma_f32_32x32x16_bf16 v[82:97], v[182:185], v[124:127], v[82:97]
	v_mfma_f32_32x32x16_bf16 v[66:81], v[66:69], v[128:131], 0
	ds_read_b128 v[128:131], v202 offset:24576
	ds_read_b128 v[240:243], v202 offset:36864
	v_mfma_f32_32x32x16_bf16 v[82:97], v[230:233], v[120:123], v[82:97]
	v_mfma_f32_32x32x16_bf16 v[66:81], v[206:209], v[124:127], v[66:81]
	ds_read_b128 v[124:127], v201 offset:24704
	ds_read_b128 v[182:185], v201 offset:36992
	s_waitcnt lgkmcnt(3)
	v_mfma_f32_32x32x16_bf16 v[82:97], v[128:131], v[116:119], v[82:97]
	v_mfma_f32_32x32x16_bf16 v[66:81], v[236:239], v[120:123], v[66:81]
	ds_read_b128 v[120:123], v203 offset:24704
	ds_read_b128 v[206:209], v203 offset:36992
	s_waitcnt lgkmcnt(3)
	v_mfma_f32_32x32x16_bf16 v[82:97], v[124:127], v[112:115], v[82:97]
	v_mfma_f32_32x32x16_bf16 v[66:81], v[240:243], v[116:119], v[66:81]
	ds_read_b128 v[116:119], v204 offset:24704
	ds_read_b128 v[128:131], v204 offset:36992
	s_waitcnt lgkmcnt(3)
	v_mfma_f32_32x32x16_bf16 v[82:97], v[120:123], v[108:111], v[82:97]
	v_mfma_f32_32x32x16_bf16 v[66:81], v[182:185], v[112:115], v[66:81]
	ds_read_b128 v[112:115], v202 offset:24704
	ds_read_b128 v[124:127], v202 offset:36992
	s_waitcnt lgkmcnt(3)
	v_mfma_f32_32x32x16_bf16 v[82:97], v[116:119], v[104:107], v[82:97]
	v_mfma_f32_32x32x16_bf16 v[66:81], v[206:209], v[108:111], v[66:81]
	ds_read_b128 v[108:111], v201 offset:24832
	ds_read_b128 v[120:123], v201 offset:37120
	s_waitcnt lgkmcnt(3)
	v_mfma_f32_32x32x16_bf16 v[82:97], v[112:115], v[100:103], v[82:97]
	v_mfma_f32_32x32x16_bf16 v[66:81], v[128:131], v[104:107], v[66:81]
	ds_read_b128 v[104:107], v203 offset:24832
	ds_read_b128 v[116:119], v203 offset:37120
	s_waitcnt lgkmcnt(3)
	v_mfma_f32_32x32x16_bf16 v[82:97], v[108:111], v[144:147], v[82:97]
	v_mfma_f32_32x32x16_bf16 v[66:81], v[124:127], v[100:103], v[66:81]
	ds_read_b128 v[100:103], v204 offset:24832
	ds_read_b128 v[112:115], v204 offset:37120
	v_exp_f32_e32 v124, v148
	v_exp_f32_e32 v125, v149
	s_waitcnt lgkmcnt(3)
	v_mfma_f32_32x32x16_bf16 v[82:97], v[104:107], v[140:143], v[82:97]
	v_mfma_f32_32x32x16_bf16 v[66:81], v[120:123], v[144:147], v[66:81]
	ds_read_b128 v[108:111], v202 offset:24832
	ds_read_b128 v[120:123], v202 offset:37120
	s_waitcnt lgkmcnt(3)
	v_mfma_f32_32x32x16_bf16 v[82:97], v[100:103], v[136:139], v[82:97]
	v_add_f32_e32 v100, 0, v169
	v_add_f32_e32 v100, v191, v100
	v_add_f32_e32 v100, v170, v100
	v_add_f32_e32 v100, v192, v100
	v_add_f32_e32 v100, v190, v100
	v_add_f32_e32 v100, v193, v100
	v_add_f32_e32 v100, v171, v100
	v_mfma_f32_32x32x16_bf16 v[66:81], v[116:119], v[140:143], v[66:81]
	v_add_f32_e32 v100, v189, v100
	v_add_f32_e32 v100, v173, v100
	v_add_f32_e32 v100, v175, v100
	v_add_f32_e32 v100, v174, v100
	v_add_f32_e32 v100, v188, v100
	v_add_f32_e32 v100, v164, v100
	v_add_f32_e32 v100, v166, v100
	s_waitcnt lgkmcnt(1)
	v_mfma_f32_32x32x16_bf16 v[82:97], v[108:111], v[132:135], v[82:97]
	v_exp_f32_e32 v110, v162
	v_exp_f32_e32 v111, v163
	v_add_f32_e32 v100, v165, v100
	v_add_f32_e32 v100, v167, v100
	v_add_f32_e32 v100, v110, v100
	v_add_f32_e32 v100, v111, v100
	v_exp_f32_e32 v116, v152
	v_mfma_f32_32x32x16_bf16 v[66:81], v[112:115], v[136:139], v[66:81]
	v_exp_f32_e32 v112, v160
	v_exp_f32_e32 v113, v161
	v_exp_f32_e32 v114, v156
	v_exp_f32_e32 v115, v157
	v_add_f32_e32 v100, v112, v100
	v_exp_f32_e32 v117, v153
	v_add_f32_e32 v100, v113, v100
	v_exp_f32_e32 v118, v150
	v_add_f32_e32 v100, v114, v100
	v_exp_f32_e32 v119, v151
	v_add_f32_e32 v100, v115, v100
	s_waitcnt lgkmcnt(0)
	v_mfma_f32_32x32x16_bf16 v[66:81], v[120:123], v[132:135], v[66:81]
	v_exp_f32_e32 v120, v158
	v_add_f32_e32 v100, v116, v100
	v_exp_f32_e32 v121, v159
	v_add_f32_e32 v100, v117, v100
	v_exp_f32_e32 v122, v154
	v_add_f32_e32 v100, v118, v100
	v_exp_f32_e32 v123, v155
	v_add_f32_e32 v100, v119, v100
	v_add_f32_e32 v100, v120, v100
	v_add_f32_e32 v100, v121, v100
	v_add_f32_e32 v100, v122, v100
	v_add_f32_e32 v100, v123, v100
	v_add_f32_e32 v100, v124, v100
	v_add_f32_e32 v104, v125, v100
	v_mov_b32_e32 v105, v104
	v_cvt_pk_bf16_f32 v100, v169, v191
	v_cvt_pk_bf16_f32 v101, v170, v192
	v_cvt_pk_bf16_f32 v102, v190, v193
	v_cvt_pk_bf16_f32 v103, v171, v189
	s_nop 1
	v_permlane32_swap_b32_e32 v104, v105
	v_permlane32_swap_b32_e32 v100, v102
	v_permlane32_swap_b32_e32 v101, v103
	v_cvt_pk_bf16_f32 v106, v173, v175
	v_cvt_pk_bf16_f32 v107, v174, v188
	v_cvt_pk_bf16_f32 v108, v164, v166
	v_cvt_pk_bf16_f32 v109, v165, v167
	v_cvt_pk_bf16_f32 v110, v110, v111
	v_cvt_pk_bf16_f32 v111, v112, v113
	v_cvt_pk_bf16_f32 v112, v114, v115
	v_cvt_pk_bf16_f32 v113, v116, v117
	v_cvt_pk_bf16_f32 v114, v118, v119
	v_cvt_pk_bf16_f32 v115, v120, v121
	v_cvt_pk_bf16_f32 v116, v122, v123
	v_cvt_pk_bf16_f32 v117, v124, v125
	s_nop 0
	v_permlane32_swap_b32_e32 v106, v108
	v_permlane32_swap_b32_e32 v107, v109
	v_permlane32_swap_b32_e32 v110, v112
	v_permlane32_swap_b32_e32 v111, v113
	v_permlane32_swap_b32_e32 v114, v116
	v_permlane32_swap_b32_e32 v115, v117
	ds_read_b64_tr_b16 v[118:119], v200 offset:0
	ds_read_b64_tr_b16 v[120:121], v200 offset:0x800
	ds_read_b64_tr_b16 v[122:123], v200 offset:0x1000
	ds_read_b64_tr_b16 v[124:125], v200 offset:0x1800
	ds_read_b64_tr_b16 v[126:127], v200 offset:0x2000
	ds_read_b64_tr_b16 v[128:129], v200 offset:0x2800
	ds_read_b64_tr_b16 v[130:131], v200 offset:0x3000
	ds_read_b64_tr_b16 v[132:133], v200 offset:0x3800
	s_waitcnt lgkmcnt(0)
	s_nop 0
	v_mfma_f32_32x32x16_bf16 v[2:17], v[100:103], v[118:121], v[2:17]
	ds_read_b64_tr_b16 v[118:119], v200 offset:0x200
	ds_read_b64_tr_b16 v[120:121], v200 offset:0xa00
	v_mfma_f32_32x32x16_bf16 v[2:17], v[106:109], v[122:125], v[2:17]
	ds_read_b64_tr_b16 v[122:123], v200 offset:0x1200
	ds_read_b64_tr_b16 v[124:125], v200 offset:0x1a00
	v_mfma_f32_32x32x16_bf16 v[2:17], v[110:113], v[126:129], v[2:17]
	ds_read_b64_tr_b16 v[126:127], v200 offset:0x2200
	ds_read_b64_tr_b16 v[128:129], v200 offset:0x2a00
	v_mfma_f32_32x32x16_bf16 v[2:17], v[114:117], v[130:133], v[2:17]
	ds_read_b64_tr_b16 v[130:131], v200 offset:0x3200
	ds_read_b64_tr_b16 v[132:133], v200 offset:0x3a00
	s_waitcnt lgkmcnt(0)
	v_mfma_f32_32x32x16_bf16 v[50:65], v[100:103], v[118:121], v[50:65]
	ds_read_b64_tr_b16 v[118:119], v200 offset:0x400
	ds_read_b64_tr_b16 v[120:121], v200 offset:0xc00
	v_mfma_f32_32x32x16_bf16 v[50:65], v[106:109], v[122:125], v[50:65]
	ds_read_b64_tr_b16 v[122:123], v200 offset:0x1400
	ds_read_b64_tr_b16 v[124:125], v200 offset:0x1c00
	v_mfma_f32_32x32x16_bf16 v[50:65], v[110:113], v[126:129], v[50:65]
	ds_read_b64_tr_b16 v[126:127], v200 offset:0x2400
	ds_read_b64_tr_b16 v[128:129], v200 offset:0x2c00
	v_mfma_f32_32x32x16_bf16 v[50:65], v[114:117], v[130:133], v[50:65]
	ds_read_b64_tr_b16 v[130:131], v200 offset:0x3400
	ds_read_b64_tr_b16 v[132:133], v200 offset:0x3c00
	s_waitcnt lgkmcnt(0)
	v_mfma_f32_32x32x16_bf16 v[34:49], v[100:103], v[118:121], v[34:49]
	ds_read_b64_tr_b16 v[118:119], v200 offset:0x600
	ds_read_b64_tr_b16 v[120:121], v200 offset:0xe00
	v_mfma_f32_32x32x16_bf16 v[34:49], v[106:109], v[122:125], v[34:49]
	ds_read_b64_tr_b16 v[122:123], v200 offset:0x1600
	ds_read_b64_tr_b16 v[124:125], v200 offset:0x1e00
	v_mfma_f32_32x32x16_bf16 v[34:49], v[110:113], v[126:129], v[34:49]
	ds_read_b64_tr_b16 v[126:127], v200 offset:0x2600
	ds_read_b64_tr_b16 v[128:129], v200 offset:0x2e00
	v_mfma_f32_32x32x16_bf16 v[34:49], v[114:117], v[130:133], v[34:49]
	ds_read_b64_tr_b16 v[130:131], v200 offset:0x3600
	ds_read_b64_tr_b16 v[132:133], v200 offset:0x3e00
	s_waitcnt lgkmcnt(0)
	v_mfma_f32_32x32x16_bf16 v[18:33], v[100:103], v[118:121], v[18:33]
	v_max_f32_e32 v100, v83, v83
	v_max_f32_e32 v101, v82, v82
	v_max_f32_e32 v100, v101, v100
	v_max3_f32 v100, v100, v84, v85
	v_max3_f32 v100, v100, v86, v87
	v_max3_f32 v100, v100, v88, v89
	v_max3_f32 v100, v100, v90, v91
	v_max3_f32 v100, v100, v92, v93
	v_max3_f32 v100, v100, v94, v95
	v_mfma_f32_32x32x16_bf16 v[18:33], v[106:109], v[122:125], v[18:33]
	v_max3_f32 v100, v100, v96, v97
	v_max3_f32 v100, v100, v66, v67
	v_max3_f32 v100, v100, v68, v69
	v_max3_f32 v100, v100, v70, v71
	v_max3_f32 v100, v100, v72, v73
	v_max3_f32 v100, v100, v74, v75
	v_max3_f32 v100, v100, v76, v77
	v_max3_f32 v100, v100, v78, v79
	v_mfma_f32_32x32x16_bf16 v[18:33], v[110:113], v[126:129], v[18:33]
	v_max3_f32 v100, v100, v80, v81
	v_mov_b32_e32 v101, v100
	s_nop 1
	v_permlane32_swap_b32_e32 v100, v101
	v_max_f32_e32 v101, v101, v101
	v_max_f32_e32 v100, v100, v100
	v_max_f32_e32 v100, v100, v101
	v_sub_f32_e32 v101, v100, v211
	v_cmp_ge_f32_e32 vcc, s11, v101
	v_max_f32_e32 v101, v211, v211
	v_max_f32_e32 v100, v101, v100
	v_mfma_f32_32x32x16_bf16 v[18:33], v[114:117], v[130:133], v[18:33]
	v_sub_f32_e32 v101, v211, v100
	v_mul_f32_e32 v101, 0x3dd53b94, v101
	v_exp_f32_e32 v101, v101
	s_cmp_eq_u64 vcc, exec
	s_cselect_b64 s[18:19], -1, 0
	v_mov_b32_e32 v229, v228
	v_cndmask_b32_e64 v102, v101, 1.0, s[18:19]
	v_cmp_gt_f32_e32 vcc, 1.0, v102
	s_waitcnt vmcnt(0)
	s_barrier
	s_cbranch_vccz .LBB0_1360
	s_and_saveexec_b64 s[4:5], s[0:1]
	ds_write_b32 v197, v102 offset:128
	s_or_b64 exec, exec, s[4:5]
	s_waitcnt lgkmcnt(0)
	v_add_u32_e32 v101, v196, v98
	ds_read_b128 v[106:109], v101 offset:224
	ds_read_b128 v[110:113], v101 offset:192
	ds_read_b128 v[114:117], v101 offset:160
	ds_read_b128 v[118:121], v101 offset:128
	s_waitcnt lgkmcnt(3)
	v_pk_mul_f32 v[14:15], v[14:15], v[106:107]
	s_waitcnt lgkmcnt(2)
	v_pk_mul_f32 v[10:11], v[10:11], v[110:111]
	s_waitcnt lgkmcnt(1)
	v_pk_mul_f32 v[6:7], v[6:7], v[114:115]
	v_pk_mul_f32 v[16:17], v[16:17], v[108:109]
	v_pk_mul_f32 v[12:13], v[12:13], v[112:113]
	v_pk_mul_f32 v[8:9], v[8:9], v[116:117]
	s_waitcnt lgkmcnt(0)
	v_pk_mul_f32 v[4:5], v[4:5], v[120:121]
	v_pk_mul_f32 v[2:3], v[2:3], v[118:119]
	v_pk_mul_f32 v[62:63], v[62:63], v[106:107]
	v_pk_mul_f32 v[58:59], v[58:59], v[110:111]
	v_pk_mul_f32 v[54:55], v[54:55], v[114:115]
	v_pk_mul_f32 v[64:65], v[64:65], v[108:109]
	v_pk_mul_f32 v[60:61], v[60:61], v[112:113]
	v_pk_mul_f32 v[56:57], v[56:57], v[116:117]
	v_pk_mul_f32 v[52:53], v[52:53], v[120:121]
	v_pk_mul_f32 v[50:51], v[50:51], v[118:119]
	v_pk_mul_f32 v[46:47], v[46:47], v[106:107]
	v_pk_mul_f32 v[42:43], v[42:43], v[110:111]
	v_pk_mul_f32 v[38:39], v[38:39], v[114:115]
	v_pk_mul_f32 v[48:49], v[48:49], v[108:109]
	v_pk_mul_f32 v[44:45], v[44:45], v[112:113]
	v_pk_mul_f32 v[40:41], v[40:41], v[116:117]
	v_pk_mul_f32 v[36:37], v[36:37], v[120:121]
	v_pk_mul_f32 v[34:35], v[34:35], v[118:119]
	v_pk_mul_f32 v[30:31], v[30:31], v[106:107]
	v_pk_mul_f32 v[26:27], v[26:27], v[110:111]
	v_pk_mul_f32 v[22:23], v[22:23], v[114:115]
	v_pk_mul_f32 v[32:33], v[32:33], v[108:109]
	v_pk_mul_f32 v[28:29], v[28:29], v[112:113]
	v_pk_mul_f32 v[24:25], v[24:25], v[116:117]
	v_pk_mul_f32 v[20:21], v[20:21], v[120:121]
	v_pk_mul_f32 v[18:19], v[18:19], v[118:119]
